# pipelined attention with re-balanced softmax quarters (20/22/20/20 ops)
# baseline (speedup 1.0000x reference)
.LBB0_734:
	s_waitcnt lgkmcnt(0)
	s_barrier
	ds_read_b128 v[160:163], v201 offset:16384
	ds_read_b128 v[164:167], v209 offset:0
	ds_read_b128 v[168:171], v202 offset:16384
	ds_read_b128 v[172:175], v209 offset:2048
	ds_read_b128 v[176:179], v203 offset:16384
	ds_read_b128 v[180:183], v209 offset:4096
	ds_read_b128 v[230:233], v246 offset:16384
	s_waitcnt lgkmcnt(6)
	v_mfma_f32_16x16x32_bf16 v[64:67], v[160:163], v[96:99], 0
	v_exp_f32_e32 v88, v88
	v_exp_f32_e32 v92, v92
	v_mfma_f32_16x16x32_bf16 v[68:71], v[160:163], v[112:115], 0
	v_cvt_pk_bf16_f32 v242, v80, v81
	v_exp_f32_e32 v89, v89
	ds_read_b128 v[234:237], v209 offset:6144
	s_add_u32 s16, s22, s10
	s_addc_u32 s17, s23, s11
	s_add_u32 s15, s22, s12
	s_addc_u32 s14, s23, s13
	s_add_u32 s8, s16, 0x3bc00200
	s_addc_u32 s9, s17, 0
	s_add_u32 s6, s15, 0x23a50000
	s_addc_u32 s7, s14, 0
	s_waitcnt lgkmcnt(6)
	v_mfma_f32_16x16x32_bf16 v[0:3], v[164:167], v[216:219], v[0:3]
	v_exp_f32_e32 v93, v93
	v_cvt_pk_bf16_f32 v243, v82, v83
	v_mfma_f32_16x16x32_bf16 v[4:7], v[164:167], v[238:241], v[4:7]
	v_exp_f32_e32 v90, v90
	v_exp_f32_e32 v94, v94
	ds_read_b128 v[160:163], v201 offset:20480
	s_waitcnt vmcnt(4)
	ds_write_b128 v225, v[152:155] offset:49152
	s_waitcnt lgkmcnt(7)
	v_mfma_f32_16x16x32_bf16 v[68:71], v[168:171], v[116:119], v[68:71]
	v_cvt_pk_bf16_f32 v204, v84, v85
	v_mfma_f32_16x16x32_bf16 v[64:67], v[168:171], v[100:103], v[64:67]
	v_exp_f32_e32 v91, v91
	ds_read_b128 v[164:167], v209 offset:8192
	ds_write_b128 v226, v[156:159] offset:49152
	s_waitcnt lgkmcnt(8)
	v_mfma_f32_16x16x32_bf16 v[12:15], v[172:175], v[238:241], v[12:15]
	v_exp_f32_e32 v95, v95
	v_mfma_f32_16x16x32_bf16 v[8:11], v[172:175], v[216:219], v[8:11]
	v_cvt_pk_bf16_f32 v205, v86, v87
	ds_read_b128 v[168:171], v202 offset:20480
	ds_write_b64 v227, v[132:133] offset:32768
	s_waitcnt lgkmcnt(9)
	v_mfma_f32_16x16x32_bf16 v[64:67], v[176:179], v[104:107], v[64:67]
	v_add_f32_e32 v220, v220, v88
	v_mfma_f32_16x16x32_bf16 v[68:71], v[176:179], v[120:123], v[68:71]
	v_add_f32_e32 v221, v221, v92
	ds_read_b128 v[172:175], v209 offset:10240
	ds_write_b64 v228, v[134:135] offset:32768
	s_waitcnt lgkmcnt(10)
	v_mfma_f32_16x16x32_bf16 v[16:19], v[180:183], v[216:219], v[16:19]
	v_add_f32_e32 v220, v220, v89
	v_mfma_f32_16x16x32_bf16 v[20:23], v[180:183], v[238:241], v[20:23]
	v_add_f32_e32 v221, v221, v93
	ds_read_b128 v[176:179], v203 offset:20480
	ds_write_b64 v229, v[128:129] offset:32768
	s_waitcnt lgkmcnt(11)
	v_mfma_f32_16x16x32_bf16 v[68:71], v[230:233], v[124:127], v[68:71]
	v_cvt_pk_bf16_f32 v244, v88, v89
	v_mfma_f32_16x16x32_bf16 v[64:67], v[230:233], v[108:111], v[64:67]
	v_cvt_pk_bf16_f32 v245, v90, v91
	ds_read_b128 v[180:183], v209 offset:12288
	ds_write_b64 v184, v[130:131] offset:32768
	s_waitcnt lgkmcnt(12)
	v_mfma_f32_16x16x32_bf16 v[28:31], v[234:237], v[238:241], v[28:31]
	v_cvt_pk_bf16_f32 v206, v92, v93
	v_mfma_f32_16x16x32_bf16 v[24:27], v[234:237], v[216:219], v[24:27]
	v_cvt_pk_bf16_f32 v207, v94, v95
	ds_read_b128 v[230:233], v246 offset:20480
	global_load_dwordx4 v[132:135], v198, s[8:9]
	s_waitcnt lgkmcnt(12)
	v_mfma_f32_16x16x32_bf16 v[72:75], v[160:163], v[96:99], 0
	v_add_f32_e32 v220, v220, v90
	v_add_f32_e32 v221, v221, v94
	v_mfma_f32_16x16x32_bf16 v[76:79], v[160:163], v[112:115], 0
	v_add_f32_e32 v220, v220, v91
	v_add_f32_e32 v221, v221, v95
	ds_read_b128 v[234:237], v209 offset:14336
	global_load_dwordx4 v[128:131], v199, s[8:9]
	s_waitcnt lgkmcnt(11)
	v_mfma_f32_16x16x32_bf16 v[32:35], v[164:167], v[216:219], v[32:35]
	v_add_f32_e32 v194, v194, v220
	v_add_f32_e32 v195, v195, v221
	v_mfma_f32_16x16x32_bf16 v[36:39], v[164:167], v[238:241], v[36:39]
	v_exp_f32_e32 v64, v64
	v_exp_f32_e32 v68, v68
	ds_read_b128 v[160:163], v201 offset:24576
	global_load_dwordx4 v[152:155], v196, s[6:7]
	s_waitcnt lgkmcnt(10)
	v_mfma_f32_16x16x32_bf16 v[76:79], v[168:171], v[116:119], v[76:79]
	v_exp_f32_e32 v65, v65
	v_mfma_f32_16x16x32_bf16 v[72:75], v[168:171], v[100:103], v[72:75]
	v_exp_f32_e32 v69, v69
	ds_read_b128 v[164:167], v210 offset:0
	global_load_dwordx4 v[156:159], v197, s[6:7]
	s_waitcnt lgkmcnt(9)
	v_mfma_f32_16x16x32_bf16 v[44:47], v[172:175], v[238:241], v[44:47]
	v_exp_f32_e32 v66, v66
	v_mfma_f32_16x16x32_bf16 v[40:43], v[172:175], v[216:219], v[40:43]
	v_exp_f32_e32 v70, v70
	ds_read_b128 v[168:171], v202 offset:24576
	s_waitcnt lgkmcnt(8)
	v_mfma_f32_16x16x32_bf16 v[72:75], v[176:179], v[104:107], v[72:75]
	v_exp_f32_e32 v67, v67
	v_mfma_f32_16x16x32_bf16 v[76:79], v[176:179], v[120:123], v[76:79]
	v_exp_f32_e32 v71, v71
	ds_read_b128 v[172:175], v210 offset:2048
	s_waitcnt lgkmcnt(7)
	v_mfma_f32_16x16x32_bf16 v[48:51], v[180:183], v[216:219], v[48:51]
	v_add_f32_e32 v220, v64, v65
	v_mfma_f32_16x16x32_bf16 v[52:55], v[180:183], v[238:241], v[52:55]
	v_add_f32_e32 v221, v68, v69
	ds_read_b128 v[176:179], v203 offset:24576
	s_waitcnt lgkmcnt(6)
	v_mfma_f32_16x16x32_bf16 v[76:79], v[230:233], v[124:127], v[76:79]
	v_add_f32_e32 v220, v220, v66
	v_mfma_f32_16x16x32_bf16 v[72:75], v[230:233], v[108:111], v[72:75]
	v_add_f32_e32 v221, v221, v70
	ds_read_b128 v[180:183], v210 offset:4096
	s_waitcnt lgkmcnt(6)
	v_mfma_f32_16x16x32_bf16 v[60:63], v[234:237], v[238:241], v[60:63]
	v_add_f32_e32 v220, v220, v67
	v_mfma_f32_16x16x32_bf16 v[56:59], v[234:237], v[216:219], v[56:59]
	v_add_f32_e32 v221, v221, v71
	ds_read_b128 v[230:233], v246 offset:24576
	s_waitcnt lgkmcnt(6)
	v_mfma_f32_16x16x32_bf16 v[80:83], v[160:163], v[96:99], 0
	v_exp_f32_e32 v72, v72
	v_exp_f32_e32 v76, v76
	v_mfma_f32_16x16x32_bf16 v[84:87], v[160:163], v[112:115], 0
	v_exp_f32_e32 v73, v73
	v_exp_f32_e32 v77, v77
	ds_read_b128 v[234:237], v210 offset:6144
	s_waitcnt lgkmcnt(6)
	v_mfma_f32_16x16x32_bf16 v[0:3], v[164:167], v[242:245], v[0:3]
	v_exp_f32_e32 v74, v74
	v_exp_f32_e32 v78, v78
	v_mfma_f32_16x16x32_bf16 v[4:7], v[164:167], v[204:207], v[4:7]
	v_exp_f32_e32 v75, v75
	v_exp_f32_e32 v79, v79
	ds_read_b128 v[160:163], v201 offset:28672
	s_waitcnt lgkmcnt(6)
	v_mfma_f32_16x16x32_bf16 v[84:87], v[168:171], v[116:119], v[84:87]
	v_add_f32_e32 v220, v220, v72
	v_mfma_f32_16x16x32_bf16 v[80:83], v[168:171], v[100:103], v[80:83]
	v_add_f32_e32 v221, v221, v76
	ds_read_b128 v[164:167], v210 offset:8192
	s_waitcnt lgkmcnt(6)
	v_mfma_f32_16x16x32_bf16 v[12:15], v[172:175], v[204:207], v[12:15]
	v_add_f32_e32 v220, v220, v73
	v_mfma_f32_16x16x32_bf16 v[8:11], v[172:175], v[242:245], v[8:11]
	v_add_f32_e32 v221, v221, v77
	ds_read_b128 v[168:171], v202 offset:28672
	s_waitcnt lgkmcnt(6)
	v_mfma_f32_16x16x32_bf16 v[80:83], v[176:179], v[104:107], v[80:83]
	v_add_f32_e32 v220, v220, v74
	v_mfma_f32_16x16x32_bf16 v[84:87], v[176:179], v[120:123], v[84:87]
	v_add_f32_e32 v221, v221, v78
	ds_read_b128 v[172:175], v210 offset:10240
	s_waitcnt lgkmcnt(6)
	v_mfma_f32_16x16x32_bf16 v[16:19], v[180:183], v[242:245], v[16:19]
	v_add_f32_e32 v220, v220, v75
	v_mfma_f32_16x16x32_bf16 v[20:23], v[180:183], v[204:207], v[20:23]
	v_add_f32_e32 v221, v221, v79
	ds_read_b128 v[176:179], v203 offset:28672
	s_waitcnt lgkmcnt(6)
	v_mfma_f32_16x16x32_bf16 v[84:87], v[230:233], v[124:127], v[84:87]
	v_cvt_pk_bf16_f32 v216, v64, v65
	v_mfma_f32_16x16x32_bf16 v[80:83], v[230:233], v[108:111], v[80:83]
	v_cvt_pk_bf16_f32 v217, v66, v67
	ds_read_b128 v[180:183], v210 offset:12288
	s_waitcnt lgkmcnt(6)
	v_mfma_f32_16x16x32_bf16 v[28:31], v[234:237], v[204:207], v[28:31]
	v_cvt_pk_bf16_f32 v238, v68, v69
	v_mfma_f32_16x16x32_bf16 v[24:27], v[234:237], v[242:245], v[24:27]
	v_cvt_pk_bf16_f32 v239, v70, v71
	ds_read_b128 v[230:233], v246 offset:28672
	s_waitcnt lgkmcnt(6)
	v_mfma_f32_16x16x32_bf16 v[88:91], v[160:163], v[96:99], 0
	v_exp_f32_e32 v80, v80
	v_exp_f32_e32 v84, v84
	v_mfma_f32_16x16x32_bf16 v[92:95], v[160:163], v[112:115], 0
	v_exp_f32_e32 v81, v81
	v_exp_f32_e32 v85, v85
	ds_read_b128 v[234:237], v210 offset:14336
	s_waitcnt lgkmcnt(6)
	v_mfma_f32_16x16x32_bf16 v[32:35], v[164:167], v[242:245], v[32:35]
	v_exp_f32_e32 v82, v82
	v_exp_f32_e32 v86, v86
	v_mfma_f32_16x16x32_bf16 v[36:39], v[164:167], v[204:207], v[36:39]
	v_exp_f32_e32 v83, v83
	v_exp_f32_e32 v87, v87
	ds_read_b128 v[160:163], v201 offset:32768
	s_waitcnt lgkmcnt(6)
	v_mfma_f32_16x16x32_bf16 v[92:95], v[168:171], v[116:119], v[92:95]
	v_add_f32_e32 v220, v220, v80
	v_mfma_f32_16x16x32_bf16 v[88:91], v[168:171], v[100:103], v[88:91]
	v_add_f32_e32 v221, v221, v84
	ds_read_b128 v[164:167], v209 offset:16384
	s_waitcnt lgkmcnt(6)
	v_mfma_f32_16x16x32_bf16 v[44:47], v[172:175], v[204:207], v[44:47]
	v_add_f32_e32 v220, v220, v81
	v_mfma_f32_16x16x32_bf16 v[40:43], v[172:175], v[242:245], v[40:43]
	v_add_f32_e32 v221, v221, v85
	ds_read_b128 v[168:171], v202 offset:32768
	s_waitcnt lgkmcnt(6)
	v_mfma_f32_16x16x32_bf16 v[88:91], v[176:179], v[104:107], v[88:91]
	v_add_f32_e32 v220, v220, v82
	v_mfma_f32_16x16x32_bf16 v[92:95], v[176:179], v[120:123], v[92:95]
	v_add_f32_e32 v221, v221, v86
	ds_read_b128 v[172:175], v209 offset:18432
	s_waitcnt lgkmcnt(6)
	v_mfma_f32_16x16x32_bf16 v[48:51], v[180:183], v[242:245], v[48:51]
	v_add_f32_e32 v220, v220, v83
	v_mfma_f32_16x16x32_bf16 v[52:55], v[180:183], v[204:207], v[52:55]
	v_add_f32_e32 v221, v221, v87
	ds_read_b128 v[176:179], v203 offset:32768
	s_waitcnt lgkmcnt(6)
	v_mfma_f32_16x16x32_bf16 v[92:95], v[230:233], v[124:127], v[92:95]
	v_cvt_pk_bf16_f32 v218, v72, v73
	v_mfma_f32_16x16x32_bf16 v[88:91], v[230:233], v[108:111], v[88:91]
	v_cvt_pk_bf16_f32 v219, v74, v75
	ds_read_b128 v[180:183], v209 offset:20480
	s_waitcnt lgkmcnt(6)
	v_mfma_f32_16x16x32_bf16 v[60:63], v[234:237], v[204:207], v[60:63]
	v_cvt_pk_bf16_f32 v240, v76, v77
	v_mfma_f32_16x16x32_bf16 v[56:59], v[234:237], v[242:245], v[56:59]
	v_cvt_pk_bf16_f32 v241, v78, v79
	ds_read_b128 v[230:233], v246 offset:32768
	s_waitcnt lgkmcnt(6)
	v_mfma_f32_16x16x32_bf16 v[64:67], v[160:163], v[96:99], 0
	v_exp_f32_e32 v88, v88
	v_exp_f32_e32 v92, v92
	v_mfma_f32_16x16x32_bf16 v[68:71], v[160:163], v[112:115], 0
	v_cvt_pk_bf16_f32 v242, v80, v81
	v_exp_f32_e32 v89, v89
	ds_read_b128 v[234:237], v209 offset:22528
	s_add_u32 s8, s16, 0x3bc00280
	s_addc_u32 s9, s17, 0
	s_add_u32 s6, s15, 0x23a60000
	s_addc_u32 s7, s14, 0
	s_waitcnt lgkmcnt(6)
	v_mfma_f32_16x16x32_bf16 v[0:3], v[164:167], v[216:219], v[0:3]
	v_exp_f32_e32 v93, v93
	v_cvt_pk_bf16_f32 v243, v82, v83
	v_mfma_f32_16x16x32_bf16 v[4:7], v[164:167], v[238:241], v[4:7]
	v_exp_f32_e32 v90, v90
	v_exp_f32_e32 v94, v94
	ds_read_b128 v[160:163], v201 offset:36864
	s_waitcnt vmcnt(4)
	ds_write_b128 v225, v[136:139] offset:0
	s_waitcnt lgkmcnt(7)
	v_mfma_f32_16x16x32_bf16 v[68:71], v[168:171], v[116:119], v[68:71]
	v_cvt_pk_bf16_f32 v204, v84, v85
	v_mfma_f32_16x16x32_bf16 v[64:67], v[168:171], v[100:103], v[64:67]
	v_exp_f32_e32 v91, v91
	ds_read_b128 v[164:167], v209 offset:24576
	ds_write_b128 v226, v[140:143] offset:0
	s_waitcnt lgkmcnt(8)
	v_mfma_f32_16x16x32_bf16 v[12:15], v[172:175], v[238:241], v[12:15]
	v_exp_f32_e32 v95, v95
	v_mfma_f32_16x16x32_bf16 v[8:11], v[172:175], v[216:219], v[8:11]
	v_cvt_pk_bf16_f32 v205, v86, v87
	ds_read_b128 v[168:171], v202 offset:36864
	ds_write_b64 v227, v[148:149] offset:49152
	s_waitcnt lgkmcnt(9)
	v_mfma_f32_16x16x32_bf16 v[64:67], v[176:179], v[104:107], v[64:67]
	v_add_f32_e32 v220, v220, v88
	v_mfma_f32_16x16x32_bf16 v[68:71], v[176:179], v[120:123], v[68:71]
	v_add_f32_e32 v221, v221, v92
	ds_read_b128 v[172:175], v209 offset:26624
	ds_write_b64 v228, v[150:151] offset:49152
	s_waitcnt lgkmcnt(10)
	v_mfma_f32_16x16x32_bf16 v[16:19], v[180:183], v[216:219], v[16:19]
	v_add_f32_e32 v220, v220, v89
	v_mfma_f32_16x16x32_bf16 v[20:23], v[180:183], v[238:241], v[20:23]
	v_add_f32_e32 v221, v221, v93
	ds_read_b128 v[176:179], v203 offset:36864
	ds_write_b64 v229, v[144:145] offset:49152
	s_waitcnt lgkmcnt(11)
	v_mfma_f32_16x16x32_bf16 v[68:71], v[230:233], v[124:127], v[68:71]
	v_cvt_pk_bf16_f32 v244, v88, v89
	v_mfma_f32_16x16x32_bf16 v[64:67], v[230:233], v[108:111], v[64:67]
	v_cvt_pk_bf16_f32 v245, v90, v91
	ds_read_b128 v[180:183], v209 offset:28672
	ds_write_b64 v184, v[146:147] offset:49152
	s_waitcnt lgkmcnt(12)
	v_mfma_f32_16x16x32_bf16 v[28:31], v[234:237], v[238:241], v[28:31]
	v_cvt_pk_bf16_f32 v206, v92, v93
	v_mfma_f32_16x16x32_bf16 v[24:27], v[234:237], v[216:219], v[24:27]
	v_cvt_pk_bf16_f32 v207, v94, v95
	ds_read_b128 v[230:233], v246 offset:36864
	global_load_dwordx4 v[148:151], v198, s[8:9]
	s_waitcnt lgkmcnt(12)
	v_mfma_f32_16x16x32_bf16 v[72:75], v[160:163], v[96:99], 0
	v_add_f32_e32 v220, v220, v90
	v_add_f32_e32 v221, v221, v94
	v_mfma_f32_16x16x32_bf16 v[76:79], v[160:163], v[112:115], 0
	v_add_f32_e32 v220, v220, v91
	v_add_f32_e32 v221, v221, v95
	ds_read_b128 v[234:237], v209 offset:30720
	global_load_dwordx4 v[144:147], v199, s[8:9]
	s_waitcnt lgkmcnt(11)
	v_mfma_f32_16x16x32_bf16 v[32:35], v[164:167], v[216:219], v[32:35]
	v_add_f32_e32 v194, v194, v220
	v_add_f32_e32 v195, v195, v221
	v_mfma_f32_16x16x32_bf16 v[36:39], v[164:167], v[238:241], v[36:39]
	v_exp_f32_e32 v64, v64
	v_exp_f32_e32 v68, v68
	ds_read_b128 v[160:163], v201 offset:40960
	global_load_dwordx4 v[136:139], v196, s[6:7]
	s_waitcnt lgkmcnt(10)
	v_mfma_f32_16x16x32_bf16 v[76:79], v[168:171], v[116:119], v[76:79]
	v_exp_f32_e32 v65, v65
	v_mfma_f32_16x16x32_bf16 v[72:75], v[168:171], v[100:103], v[72:75]
	v_exp_f32_e32 v69, v69
	ds_read_b128 v[164:167], v210 offset:16384
	global_load_dwordx4 v[140:143], v197, s[6:7]
	s_waitcnt lgkmcnt(9)
	v_mfma_f32_16x16x32_bf16 v[44:47], v[172:175], v[238:241], v[44:47]
	v_exp_f32_e32 v66, v66
	v_mfma_f32_16x16x32_bf16 v[40:43], v[172:175], v[216:219], v[40:43]
	v_exp_f32_e32 v70, v70
	ds_read_b128 v[168:171], v202 offset:40960
	s_waitcnt lgkmcnt(8)
	v_mfma_f32_16x16x32_bf16 v[72:75], v[176:179], v[104:107], v[72:75]
	v_exp_f32_e32 v67, v67
	v_mfma_f32_16x16x32_bf16 v[76:79], v[176:179], v[120:123], v[76:79]
	v_exp_f32_e32 v71, v71
	ds_read_b128 v[172:175], v210 offset:18432
	s_waitcnt lgkmcnt(7)
	v_mfma_f32_16x16x32_bf16 v[48:51], v[180:183], v[216:219], v[48:51]
	v_add_f32_e32 v220, v64, v65
	v_mfma_f32_16x16x32_bf16 v[52:55], v[180:183], v[238:241], v[52:55]
	v_add_f32_e32 v221, v68, v69
	ds_read_b128 v[176:179], v203 offset:40960
	s_waitcnt lgkmcnt(6)
	v_mfma_f32_16x16x32_bf16 v[76:79], v[230:233], v[124:127], v[76:79]
	v_add_f32_e32 v220, v220, v66
	v_mfma_f32_16x16x32_bf16 v[72:75], v[230:233], v[108:111], v[72:75]
	v_add_f32_e32 v221, v221, v70
	ds_read_b128 v[180:183], v210 offset:20480
	s_waitcnt lgkmcnt(6)
	v_mfma_f32_16x16x32_bf16 v[60:63], v[234:237], v[238:241], v[60:63]
	v_add_f32_e32 v220, v220, v67
	v_mfma_f32_16x16x32_bf16 v[56:59], v[234:237], v[216:219], v[56:59]
	v_add_f32_e32 v221, v221, v71
	ds_read_b128 v[230:233], v246 offset:40960
	s_waitcnt lgkmcnt(6)
	v_mfma_f32_16x16x32_bf16 v[80:83], v[160:163], v[96:99], 0
	v_exp_f32_e32 v72, v72
	v_exp_f32_e32 v76, v76
	v_mfma_f32_16x16x32_bf16 v[84:87], v[160:163], v[112:115], 0
	v_exp_f32_e32 v73, v73
	v_exp_f32_e32 v77, v77
	ds_read_b128 v[234:237], v210 offset:22528
	s_waitcnt lgkmcnt(6)
	v_mfma_f32_16x16x32_bf16 v[0:3], v[164:167], v[242:245], v[0:3]
	v_exp_f32_e32 v74, v74
	v_exp_f32_e32 v78, v78
	v_mfma_f32_16x16x32_bf16 v[4:7], v[164:167], v[204:207], v[4:7]
	v_exp_f32_e32 v75, v75
	v_exp_f32_e32 v79, v79
	ds_read_b128 v[160:163], v201 offset:45056
	s_waitcnt lgkmcnt(6)
	v_mfma_f32_16x16x32_bf16 v[84:87], v[168:171], v[116:119], v[84:87]
	v_add_f32_e32 v220, v220, v72
	v_mfma_f32_16x16x32_bf16 v[80:83], v[168:171], v[100:103], v[80:83]
	v_add_f32_e32 v221, v221, v76
	ds_read_b128 v[164:167], v210 offset:24576
	s_waitcnt lgkmcnt(6)
	v_mfma_f32_16x16x32_bf16 v[12:15], v[172:175], v[204:207], v[12:15]
	v_add_f32_e32 v220, v220, v73
	v_mfma_f32_16x16x32_bf16 v[8:11], v[172:175], v[242:245], v[8:11]
	v_add_f32_e32 v221, v221, v77
	ds_read_b128 v[168:171], v202 offset:45056
	s_waitcnt lgkmcnt(6)
	v_mfma_f32_16x16x32_bf16 v[80:83], v[176:179], v[104:107], v[80:83]
	v_add_f32_e32 v220, v220, v74
	v_mfma_f32_16x16x32_bf16 v[84:87], v[176:179], v[120:123], v[84:87]
	v_add_f32_e32 v221, v221, v78
	ds_read_b128 v[172:175], v210 offset:26624
	s_waitcnt lgkmcnt(6)
	v_mfma_f32_16x16x32_bf16 v[16:19], v[180:183], v[242:245], v[16:19]
	v_add_f32_e32 v220, v220, v75
	v_mfma_f32_16x16x32_bf16 v[20:23], v[180:183], v[204:207], v[20:23]
	v_add_f32_e32 v221, v221, v79
	ds_read_b128 v[176:179], v203 offset:45056
	s_waitcnt lgkmcnt(6)
	v_mfma_f32_16x16x32_bf16 v[84:87], v[230:233], v[124:127], v[84:87]
	v_cvt_pk_bf16_f32 v216, v64, v65
	v_mfma_f32_16x16x32_bf16 v[80:83], v[230:233], v[108:111], v[80:83]
	v_cvt_pk_bf16_f32 v217, v66, v67
	ds_read_b128 v[180:183], v210 offset:28672
	s_waitcnt lgkmcnt(6)
	v_mfma_f32_16x16x32_bf16 v[28:31], v[234:237], v[204:207], v[28:31]
	v_cvt_pk_bf16_f32 v238, v68, v69
	v_mfma_f32_16x16x32_bf16 v[24:27], v[234:237], v[242:245], v[24:27]
	v_cvt_pk_bf16_f32 v239, v70, v71
	ds_read_b128 v[230:233], v246 offset:45056
	s_waitcnt lgkmcnt(6)
	v_mfma_f32_16x16x32_bf16 v[88:91], v[160:163], v[96:99], 0
	v_exp_f32_e32 v80, v80
	v_exp_f32_e32 v84, v84
	v_mfma_f32_16x16x32_bf16 v[92:95], v[160:163], v[112:115], 0
	v_exp_f32_e32 v81, v81
	v_exp_f32_e32 v85, v85
	ds_read_b128 v[234:237], v210 offset:30720
	s_waitcnt lgkmcnt(6)
	v_mfma_f32_16x16x32_bf16 v[32:35], v[164:167], v[242:245], v[32:35]
	v_exp_f32_e32 v82, v82
	v_exp_f32_e32 v86, v86
	v_mfma_f32_16x16x32_bf16 v[36:39], v[164:167], v[204:207], v[36:39]
	v_exp_f32_e32 v83, v83
	v_exp_f32_e32 v87, v87
	s_waitcnt lgkmcnt(5)
	v_mfma_f32_16x16x32_bf16 v[92:95], v[168:171], v[116:119], v[92:95]
	v_add_f32_e32 v220, v220, v80
	v_mfma_f32_16x16x32_bf16 v[88:91], v[168:171], v[100:103], v[88:91]
	v_add_f32_e32 v221, v221, v84
	s_waitcnt lgkmcnt(4)
	v_mfma_f32_16x16x32_bf16 v[44:47], v[172:175], v[204:207], v[44:47]
	v_add_f32_e32 v220, v220, v81
	v_mfma_f32_16x16x32_bf16 v[40:43], v[172:175], v[242:245], v[40:43]
	v_add_f32_e32 v221, v221, v85
	s_waitcnt lgkmcnt(3)
	v_mfma_f32_16x16x32_bf16 v[88:91], v[176:179], v[104:107], v[88:91]
	v_add_f32_e32 v220, v220, v82
	v_mfma_f32_16x16x32_bf16 v[92:95], v[176:179], v[120:123], v[92:95]
	v_add_f32_e32 v221, v221, v86
	s_waitcnt lgkmcnt(2)
	v_mfma_f32_16x16x32_bf16 v[48:51], v[180:183], v[242:245], v[48:51]
	v_add_f32_e32 v220, v220, v83
	v_mfma_f32_16x16x32_bf16 v[52:55], v[180:183], v[204:207], v[52:55]
	v_add_f32_e32 v221, v221, v87
	s_waitcnt lgkmcnt(1)
	v_mfma_f32_16x16x32_bf16 v[92:95], v[230:233], v[124:127], v[92:95]
	v_cvt_pk_bf16_f32 v218, v72, v73
	v_mfma_f32_16x16x32_bf16 v[88:91], v[230:233], v[108:111], v[88:91]
	v_cvt_pk_bf16_f32 v219, v74, v75
	s_waitcnt lgkmcnt(0)
	v_mfma_f32_16x16x32_bf16 v[60:63], v[234:237], v[204:207], v[60:63]
	v_cvt_pk_bf16_f32 v240, v76, v77
	v_mfma_f32_16x16x32_bf16 v[56:59], v[234:237], v[242:245], v[56:59]
	v_cvt_pk_bf16_f32 v241, v78, v79
	s_waitcnt lgkmcnt(0)
	s_barrier
	ds_read_b128 v[160:163], v201 offset:49152
	ds_read_b128 v[164:167], v209 offset:32768
	ds_read_b128 v[168:171], v202 offset:49152
	ds_read_b128 v[172:175], v209 offset:34816
	ds_read_b128 v[176:179], v203 offset:49152
	ds_read_b128 v[180:183], v209 offset:36864
	ds_read_b128 v[230:233], v246 offset:49152
	s_waitcnt lgkmcnt(6)
	v_mfma_f32_16x16x32_bf16 v[64:67], v[160:163], v[96:99], 0
	v_exp_f32_e32 v88, v88
	v_exp_f32_e32 v92, v92
	v_mfma_f32_16x16x32_bf16 v[68:71], v[160:163], v[112:115], 0
	v_cvt_pk_bf16_f32 v242, v80, v81
	v_exp_f32_e32 v89, v89
	ds_read_b128 v[234:237], v209 offset:38912
	s_add_u32 s8, s16, 0x3bc00300
	s_addc_u32 s9, s17, 0
	s_add_u32 s6, s15, 0x23a70000
	s_addc_u32 s7, s14, 0
	s_waitcnt lgkmcnt(6)
	v_mfma_f32_16x16x32_bf16 v[0:3], v[164:167], v[216:219], v[0:3]
	v_exp_f32_e32 v93, v93
	v_cvt_pk_bf16_f32 v243, v82, v83
	v_mfma_f32_16x16x32_bf16 v[4:7], v[164:167], v[238:241], v[4:7]
	v_exp_f32_e32 v90, v90
	v_exp_f32_e32 v94, v94
	ds_read_b128 v[160:163], v201 offset:53248
	s_waitcnt vmcnt(4)
	ds_write_b128 v225, v[152:155] offset:16384
	s_waitcnt lgkmcnt(7)
	v_mfma_f32_16x16x32_bf16 v[68:71], v[168:171], v[116:119], v[68:71]
	v_cvt_pk_bf16_f32 v204, v84, v85
	v_mfma_f32_16x16x32_bf16 v[64:67], v[168:171], v[100:103], v[64:67]
	v_exp_f32_e32 v91, v91
	ds_read_b128 v[164:167], v209 offset:40960
	ds_write_b128 v226, v[156:159] offset:16384
	s_waitcnt lgkmcnt(8)
	v_mfma_f32_16x16x32_bf16 v[12:15], v[172:175], v[238:241], v[12:15]
	v_exp_f32_e32 v95, v95
	v_mfma_f32_16x16x32_bf16 v[8:11], v[172:175], v[216:219], v[8:11]
	v_cvt_pk_bf16_f32 v205, v86, v87
	ds_read_b128 v[168:171], v202 offset:53248
	ds_write_b64 v227, v[132:133] offset:0
	s_waitcnt lgkmcnt(9)
	v_mfma_f32_16x16x32_bf16 v[64:67], v[176:179], v[104:107], v[64:67]
	v_add_f32_e32 v220, v220, v88
	v_mfma_f32_16x16x32_bf16 v[68:71], v[176:179], v[120:123], v[68:71]
	v_add_f32_e32 v221, v221, v92
	ds_read_b128 v[172:175], v209 offset:43008
	ds_write_b64 v228, v[134:135] offset:0
	s_waitcnt lgkmcnt(10)
	v_mfma_f32_16x16x32_bf16 v[16:19], v[180:183], v[216:219], v[16:19]
	v_add_f32_e32 v220, v220, v89
	v_mfma_f32_16x16x32_bf16 v[20:23], v[180:183], v[238:241], v[20:23]
	v_add_f32_e32 v221, v221, v93
	ds_read_b128 v[176:179], v203 offset:53248
	ds_write_b64 v229, v[128:129] offset:0
	s_waitcnt lgkmcnt(11)
	v_mfma_f32_16x16x32_bf16 v[68:71], v[230:233], v[124:127], v[68:71]
	v_cvt_pk_bf16_f32 v244, v88, v89
	v_mfma_f32_16x16x32_bf16 v[64:67], v[230:233], v[108:111], v[64:67]
	v_cvt_pk_bf16_f32 v245, v90, v91
	ds_read_b128 v[180:183], v209 offset:45056
	ds_write_b64 v184, v[130:131] offset:0
	s_waitcnt lgkmcnt(12)
	v_mfma_f32_16x16x32_bf16 v[28:31], v[234:237], v[238:241], v[28:31]
	v_cvt_pk_bf16_f32 v206, v92, v93
	v_mfma_f32_16x16x32_bf16 v[24:27], v[234:237], v[216:219], v[24:27]
	v_cvt_pk_bf16_f32 v207, v94, v95
	ds_read_b128 v[230:233], v246 offset:53248
	global_load_dwordx4 v[132:135], v198, s[8:9]
	s_waitcnt lgkmcnt(12)
	v_mfma_f32_16x16x32_bf16 v[72:75], v[160:163], v[96:99], 0
	v_add_f32_e32 v220, v220, v90
	v_add_f32_e32 v221, v221, v94
	v_mfma_f32_16x16x32_bf16 v[76:79], v[160:163], v[112:115], 0
	v_add_f32_e32 v220, v220, v91
	v_add_f32_e32 v221, v221, v95
	ds_read_b128 v[234:237], v209 offset:47104
	global_load_dwordx4 v[128:131], v199, s[8:9]
	s_waitcnt lgkmcnt(11)
	v_mfma_f32_16x16x32_bf16 v[32:35], v[164:167], v[216:219], v[32:35]
	v_add_f32_e32 v194, v194, v220
	v_add_f32_e32 v195, v195, v221
	v_mfma_f32_16x16x32_bf16 v[36:39], v[164:167], v[238:241], v[36:39]
	v_exp_f32_e32 v64, v64
	v_exp_f32_e32 v68, v68
	ds_read_b128 v[160:163], v201 offset:57344
	global_load_dwordx4 v[152:155], v196, s[6:7]
	s_waitcnt lgkmcnt(10)
	v_mfma_f32_16x16x32_bf16 v[76:79], v[168:171], v[116:119], v[76:79]
	v_exp_f32_e32 v65, v65
	v_mfma_f32_16x16x32_bf16 v[72:75], v[168:171], v[100:103], v[72:75]
	v_exp_f32_e32 v69, v69
	ds_read_b128 v[164:167], v210 offset:32768
	global_load_dwordx4 v[156:159], v197, s[6:7]
	s_waitcnt lgkmcnt(9)
	v_mfma_f32_16x16x32_bf16 v[44:47], v[172:175], v[238:241], v[44:47]
	v_exp_f32_e32 v66, v66
	v_mfma_f32_16x16x32_bf16 v[40:43], v[172:175], v[216:219], v[40:43]
	v_exp_f32_e32 v70, v70
	ds_read_b128 v[168:171], v202 offset:57344
	s_waitcnt lgkmcnt(8)
	v_mfma_f32_16x16x32_bf16 v[72:75], v[176:179], v[104:107], v[72:75]
	v_exp_f32_e32 v67, v67
	v_mfma_f32_16x16x32_bf16 v[76:79], v[176:179], v[120:123], v[76:79]
	v_exp_f32_e32 v71, v71
	ds_read_b128 v[172:175], v210 offset:34816
	s_waitcnt lgkmcnt(7)
	v_mfma_f32_16x16x32_bf16 v[48:51], v[180:183], v[216:219], v[48:51]
	v_add_f32_e32 v220, v64, v65
	v_mfma_f32_16x16x32_bf16 v[52:55], v[180:183], v[238:241], v[52:55]
	v_add_f32_e32 v221, v68, v69
	ds_read_b128 v[176:179], v203 offset:57344
	s_waitcnt lgkmcnt(6)
	v_mfma_f32_16x16x32_bf16 v[76:79], v[230:233], v[124:127], v[76:79]
	v_add_f32_e32 v220, v220, v66
	v_mfma_f32_16x16x32_bf16 v[72:75], v[230:233], v[108:111], v[72:75]
	v_add_f32_e32 v221, v221, v70
	ds_read_b128 v[180:183], v210 offset:36864
	s_waitcnt lgkmcnt(6)
	v_mfma_f32_16x16x32_bf16 v[60:63], v[234:237], v[238:241], v[60:63]
	v_add_f32_e32 v220, v220, v67
	v_mfma_f32_16x16x32_bf16 v[56:59], v[234:237], v[216:219], v[56:59]
	v_add_f32_e32 v221, v221, v71
	ds_read_b128 v[230:233], v246 offset:57344
	s_waitcnt lgkmcnt(6)
	v_mfma_f32_16x16x32_bf16 v[80:83], v[160:163], v[96:99], 0
	v_exp_f32_e32 v72, v72
	v_exp_f32_e32 v76, v76
	v_mfma_f32_16x16x32_bf16 v[84:87], v[160:163], v[112:115], 0
	v_exp_f32_e32 v73, v73
	v_exp_f32_e32 v77, v77
	ds_read_b128 v[234:237], v210 offset:38912
	s_waitcnt lgkmcnt(6)
	v_mfma_f32_16x16x32_bf16 v[0:3], v[164:167], v[242:245], v[0:3]
	v_exp_f32_e32 v74, v74
	v_exp_f32_e32 v78, v78
	v_mfma_f32_16x16x32_bf16 v[4:7], v[164:167], v[204:207], v[4:7]
	v_exp_f32_e32 v75, v75
	v_exp_f32_e32 v79, v79
	ds_read_b128 v[160:163], v201 offset:61440
	s_waitcnt lgkmcnt(6)
	v_mfma_f32_16x16x32_bf16 v[84:87], v[168:171], v[116:119], v[84:87]
	v_add_f32_e32 v220, v220, v72
	v_mfma_f32_16x16x32_bf16 v[80:83], v[168:171], v[100:103], v[80:83]
	v_add_f32_e32 v221, v221, v76
	ds_read_b128 v[164:167], v210 offset:40960
	s_waitcnt lgkmcnt(6)
	v_mfma_f32_16x16x32_bf16 v[12:15], v[172:175], v[204:207], v[12:15]
	v_add_f32_e32 v220, v220, v73
	v_mfma_f32_16x16x32_bf16 v[8:11], v[172:175], v[242:245], v[8:11]
	v_add_f32_e32 v221, v221, v77
	ds_read_b128 v[168:171], v202 offset:61440
	s_waitcnt lgkmcnt(6)
	v_mfma_f32_16x16x32_bf16 v[80:83], v[176:179], v[104:107], v[80:83]
	v_add_f32_e32 v220, v220, v74
	v_mfma_f32_16x16x32_bf16 v[84:87], v[176:179], v[120:123], v[84:87]
	v_add_f32_e32 v221, v221, v78
	ds_read_b128 v[172:175], v210 offset:43008
	s_waitcnt lgkmcnt(6)
	v_mfma_f32_16x16x32_bf16 v[16:19], v[180:183], v[242:245], v[16:19]
	v_add_f32_e32 v220, v220, v75
	v_mfma_f32_16x16x32_bf16 v[20:23], v[180:183], v[204:207], v[20:23]
	v_add_f32_e32 v221, v221, v79
	ds_read_b128 v[176:179], v203 offset:61440
	s_waitcnt lgkmcnt(6)
	v_mfma_f32_16x16x32_bf16 v[84:87], v[230:233], v[124:127], v[84:87]
	v_cvt_pk_bf16_f32 v216, v64, v65
	v_mfma_f32_16x16x32_bf16 v[80:83], v[230:233], v[108:111], v[80:83]
	v_cvt_pk_bf16_f32 v217, v66, v67
	ds_read_b128 v[180:183], v210 offset:45056
	s_waitcnt lgkmcnt(6)
	v_mfma_f32_16x16x32_bf16 v[28:31], v[234:237], v[204:207], v[28:31]
	v_cvt_pk_bf16_f32 v238, v68, v69
	v_mfma_f32_16x16x32_bf16 v[24:27], v[234:237], v[242:245], v[24:27]
	v_cvt_pk_bf16_f32 v239, v70, v71
	ds_read_b128 v[230:233], v246 offset:61440
	s_waitcnt lgkmcnt(6)
	v_mfma_f32_16x16x32_bf16 v[88:91], v[160:163], v[96:99], 0
	v_exp_f32_e32 v80, v80
	v_exp_f32_e32 v84, v84
	v_mfma_f32_16x16x32_bf16 v[92:95], v[160:163], v[112:115], 0
	v_exp_f32_e32 v81, v81
	v_exp_f32_e32 v85, v85
	ds_read_b128 v[234:237], v210 offset:47104
	s_waitcnt lgkmcnt(6)
	v_mfma_f32_16x16x32_bf16 v[32:35], v[164:167], v[242:245], v[32:35]
	v_exp_f32_e32 v82, v82
	v_exp_f32_e32 v86, v86
	v_mfma_f32_16x16x32_bf16 v[36:39], v[164:167], v[204:207], v[36:39]
	v_exp_f32_e32 v83, v83
	v_exp_f32_e32 v87, v87
	ds_read_b128 v[160:163], v201 offset:0
	s_waitcnt lgkmcnt(6)
	v_mfma_f32_16x16x32_bf16 v[92:95], v[168:171], v[116:119], v[92:95]
	v_add_f32_e32 v220, v220, v80
	v_mfma_f32_16x16x32_bf16 v[88:91], v[168:171], v[100:103], v[88:91]
	v_add_f32_e32 v221, v221, v84
	ds_read_b128 v[164:167], v209 offset:49152
	s_waitcnt lgkmcnt(6)
	v_mfma_f32_16x16x32_bf16 v[44:47], v[172:175], v[204:207], v[44:47]
	v_add_f32_e32 v220, v220, v81
	v_mfma_f32_16x16x32_bf16 v[40:43], v[172:175], v[242:245], v[40:43]
	v_add_f32_e32 v221, v221, v85
	ds_read_b128 v[168:171], v202 offset:0
	s_waitcnt lgkmcnt(6)
	v_mfma_f32_16x16x32_bf16 v[88:91], v[176:179], v[104:107], v[88:91]
	v_add_f32_e32 v220, v220, v82
	v_mfma_f32_16x16x32_bf16 v[92:95], v[176:179], v[120:123], v[92:95]
	v_add_f32_e32 v221, v221, v86
	ds_read_b128 v[172:175], v209 offset:51200
	s_waitcnt lgkmcnt(6)
	v_mfma_f32_16x16x32_bf16 v[48:51], v[180:183], v[242:245], v[48:51]
	v_add_f32_e32 v220, v220, v83
	v_mfma_f32_16x16x32_bf16 v[52:55], v[180:183], v[204:207], v[52:55]
	v_add_f32_e32 v221, v221, v87
	ds_read_b128 v[176:179], v203 offset:0
	s_waitcnt lgkmcnt(6)
	v_mfma_f32_16x16x32_bf16 v[92:95], v[230:233], v[124:127], v[92:95]
	v_cvt_pk_bf16_f32 v218, v72, v73
	v_mfma_f32_16x16x32_bf16 v[88:91], v[230:233], v[108:111], v[88:91]
	v_cvt_pk_bf16_f32 v219, v74, v75
	ds_read_b128 v[180:183], v209 offset:53248
	s_waitcnt lgkmcnt(6)
	v_mfma_f32_16x16x32_bf16 v[60:63], v[234:237], v[204:207], v[60:63]
	v_cvt_pk_bf16_f32 v240, v76, v77
	v_mfma_f32_16x16x32_bf16 v[56:59], v[234:237], v[242:245], v[56:59]
	v_cvt_pk_bf16_f32 v241, v78, v79
	ds_read_b128 v[230:233], v246 offset:0
	s_waitcnt lgkmcnt(6)
	v_mfma_f32_16x16x32_bf16 v[64:67], v[160:163], v[96:99], 0
	v_exp_f32_e32 v88, v88
	v_exp_f32_e32 v92, v92
	v_mfma_f32_16x16x32_bf16 v[68:71], v[160:163], v[112:115], 0
	v_cvt_pk_bf16_f32 v242, v80, v81
	v_exp_f32_e32 v89, v89
	ds_read_b128 v[234:237], v209 offset:55296
	s_add_u32 s8, s16, 0x3bc00380
	s_addc_u32 s9, s17, 0
	s_add_u32 s6, s15, 0x23a80000
	s_addc_u32 s7, s14, 0
	s_waitcnt lgkmcnt(6)
	v_mfma_f32_16x16x32_bf16 v[0:3], v[164:167], v[216:219], v[0:3]
	v_exp_f32_e32 v93, v93
	v_cvt_pk_bf16_f32 v243, v82, v83
	v_mfma_f32_16x16x32_bf16 v[4:7], v[164:167], v[238:241], v[4:7]
	v_exp_f32_e32 v90, v90
	v_exp_f32_e32 v94, v94
	ds_read_b128 v[160:163], v201 offset:4096
	s_waitcnt vmcnt(4)
	ds_write_b128 v225, v[136:139] offset:32768
	s_waitcnt lgkmcnt(7)
	v_mfma_f32_16x16x32_bf16 v[68:71], v[168:171], v[116:119], v[68:71]
	v_cvt_pk_bf16_f32 v204, v84, v85
	v_mfma_f32_16x16x32_bf16 v[64:67], v[168:171], v[100:103], v[64:67]
	v_exp_f32_e32 v91, v91
	ds_read_b128 v[164:167], v209 offset:57344
	ds_write_b128 v226, v[140:143] offset:32768
	s_waitcnt lgkmcnt(8)
	v_mfma_f32_16x16x32_bf16 v[12:15], v[172:175], v[238:241], v[12:15]
	v_exp_f32_e32 v95, v95
	v_mfma_f32_16x16x32_bf16 v[8:11], v[172:175], v[216:219], v[8:11]
	v_cvt_pk_bf16_f32 v205, v86, v87
	ds_read_b128 v[168:171], v202 offset:4096
	ds_write_b64 v227, v[148:149] offset:16384
	s_waitcnt lgkmcnt(9)
	v_mfma_f32_16x16x32_bf16 v[64:67], v[176:179], v[104:107], v[64:67]
	v_add_f32_e32 v220, v220, v88
	v_mfma_f32_16x16x32_bf16 v[68:71], v[176:179], v[120:123], v[68:71]
	v_add_f32_e32 v221, v221, v92
	ds_read_b128 v[172:175], v209 offset:59392
	ds_write_b64 v228, v[150:151] offset:16384
	s_waitcnt lgkmcnt(10)
	v_mfma_f32_16x16x32_bf16 v[16:19], v[180:183], v[216:219], v[16:19]
	v_add_f32_e32 v220, v220, v89
	v_mfma_f32_16x16x32_bf16 v[20:23], v[180:183], v[238:241], v[20:23]
	v_add_f32_e32 v221, v221, v93
	ds_read_b128 v[176:179], v203 offset:4096
	ds_write_b64 v229, v[144:145] offset:16384
	s_waitcnt lgkmcnt(11)
	v_mfma_f32_16x16x32_bf16 v[68:71], v[230:233], v[124:127], v[68:71]
	v_cvt_pk_bf16_f32 v244, v88, v89
	v_mfma_f32_16x16x32_bf16 v[64:67], v[230:233], v[108:111], v[64:67]
	v_cvt_pk_bf16_f32 v245, v90, v91
	ds_read_b128 v[180:183], v209 offset:61440
	ds_write_b64 v184, v[146:147] offset:16384
	s_waitcnt lgkmcnt(12)
	v_mfma_f32_16x16x32_bf16 v[28:31], v[234:237], v[238:241], v[28:31]
	v_cvt_pk_bf16_f32 v206, v92, v93
	v_mfma_f32_16x16x32_bf16 v[24:27], v[234:237], v[216:219], v[24:27]
	v_cvt_pk_bf16_f32 v207, v94, v95
	ds_read_b128 v[230:233], v246 offset:4096
	global_load_dwordx4 v[148:151], v198, s[8:9]
	s_waitcnt lgkmcnt(12)
	v_mfma_f32_16x16x32_bf16 v[72:75], v[160:163], v[96:99], 0
	v_add_f32_e32 v220, v220, v90
	v_add_f32_e32 v221, v221, v94
	v_mfma_f32_16x16x32_bf16 v[76:79], v[160:163], v[112:115], 0
	v_add_f32_e32 v220, v220, v91
	v_add_f32_e32 v221, v221, v95
	ds_read_b128 v[234:237], v209 offset:63488
	global_load_dwordx4 v[144:147], v199, s[8:9]
	s_waitcnt lgkmcnt(11)
	v_mfma_f32_16x16x32_bf16 v[32:35], v[164:167], v[216:219], v[32:35]
	v_add_f32_e32 v194, v194, v220
	v_add_f32_e32 v195, v195, v221
	v_mfma_f32_16x16x32_bf16 v[36:39], v[164:167], v[238:241], v[36:39]
	v_exp_f32_e32 v64, v64
	v_exp_f32_e32 v68, v68
	ds_read_b128 v[160:163], v201 offset:8192
	global_load_dwordx4 v[136:139], v196, s[6:7]
	s_waitcnt lgkmcnt(10)
	v_mfma_f32_16x16x32_bf16 v[76:79], v[168:171], v[116:119], v[76:79]
	v_exp_f32_e32 v65, v65
	v_mfma_f32_16x16x32_bf16 v[72:75], v[168:171], v[100:103], v[72:75]
	v_exp_f32_e32 v69, v69
	ds_read_b128 v[164:167], v210 offset:49152
	global_load_dwordx4 v[140:143], v197, s[6:7]
	s_waitcnt lgkmcnt(9)
	v_mfma_f32_16x16x32_bf16 v[44:47], v[172:175], v[238:241], v[44:47]
	v_exp_f32_e32 v66, v66
	v_mfma_f32_16x16x32_bf16 v[40:43], v[172:175], v[216:219], v[40:43]
	v_exp_f32_e32 v70, v70
	ds_read_b128 v[168:171], v202 offset:8192
	s_waitcnt lgkmcnt(8)
	v_mfma_f32_16x16x32_bf16 v[72:75], v[176:179], v[104:107], v[72:75]
	v_exp_f32_e32 v67, v67
	v_mfma_f32_16x16x32_bf16 v[76:79], v[176:179], v[120:123], v[76:79]
	v_exp_f32_e32 v71, v71
	ds_read_b128 v[172:175], v210 offset:51200
	s_waitcnt lgkmcnt(7)
	v_mfma_f32_16x16x32_bf16 v[48:51], v[180:183], v[216:219], v[48:51]
	v_add_f32_e32 v220, v64, v65
	v_mfma_f32_16x16x32_bf16 v[52:55], v[180:183], v[238:241], v[52:55]
	v_add_f32_e32 v221, v68, v69
	ds_read_b128 v[176:179], v203 offset:8192
	s_waitcnt lgkmcnt(6)
	v_mfma_f32_16x16x32_bf16 v[76:79], v[230:233], v[124:127], v[76:79]
	v_add_f32_e32 v220, v220, v66
	v_mfma_f32_16x16x32_bf16 v[72:75], v[230:233], v[108:111], v[72:75]
	v_add_f32_e32 v221, v221, v70
	ds_read_b128 v[180:183], v210 offset:53248
	s_waitcnt lgkmcnt(6)
	v_mfma_f32_16x16x32_bf16 v[60:63], v[234:237], v[238:241], v[60:63]
	v_add_f32_e32 v220, v220, v67
	v_mfma_f32_16x16x32_bf16 v[56:59], v[234:237], v[216:219], v[56:59]
	v_add_f32_e32 v221, v221, v71
	ds_read_b128 v[230:233], v246 offset:8192
	s_waitcnt lgkmcnt(6)
	v_mfma_f32_16x16x32_bf16 v[80:83], v[160:163], v[96:99], 0
	v_exp_f32_e32 v72, v72
	v_exp_f32_e32 v76, v76
	v_mfma_f32_16x16x32_bf16 v[84:87], v[160:163], v[112:115], 0
	v_exp_f32_e32 v73, v73
	v_exp_f32_e32 v77, v77
	ds_read_b128 v[234:237], v210 offset:55296
	s_waitcnt lgkmcnt(6)
	v_mfma_f32_16x16x32_bf16 v[0:3], v[164:167], v[242:245], v[0:3]
	v_exp_f32_e32 v74, v74
	v_exp_f32_e32 v78, v78
	v_mfma_f32_16x16x32_bf16 v[4:7], v[164:167], v[204:207], v[4:7]
	v_exp_f32_e32 v75, v75
	v_exp_f32_e32 v79, v79
	ds_read_b128 v[160:163], v201 offset:12288
	s_waitcnt lgkmcnt(6)
	v_mfma_f32_16x16x32_bf16 v[84:87], v[168:171], v[116:119], v[84:87]
	v_add_f32_e32 v220, v220, v72
	v_mfma_f32_16x16x32_bf16 v[80:83], v[168:171], v[100:103], v[80:83]
	v_add_f32_e32 v221, v221, v76
	ds_read_b128 v[164:167], v210 offset:57344
	s_waitcnt lgkmcnt(6)
	v_mfma_f32_16x16x32_bf16 v[12:15], v[172:175], v[204:207], v[12:15]
	v_add_f32_e32 v220, v220, v73
	v_mfma_f32_16x16x32_bf16 v[8:11], v[172:175], v[242:245], v[8:11]
	v_add_f32_e32 v221, v221, v77
	ds_read_b128 v[168:171], v202 offset:12288
	s_waitcnt lgkmcnt(6)
	v_mfma_f32_16x16x32_bf16 v[80:83], v[176:179], v[104:107], v[80:83]
	v_add_f32_e32 v220, v220, v74
	v_mfma_f32_16x16x32_bf16 v[84:87], v[176:179], v[120:123], v[84:87]
	v_add_f32_e32 v221, v221, v78
	ds_read_b128 v[172:175], v210 offset:59392
	s_add_u32 s10, s10, 0x200
	s_addc_u32 s11, s11, 0
	s_add_u32 s12, s12, 0x40000
	s_addc_u32 s13, s13, 0
	s_add_i32 s4, s4, 4
	s_cmpk_lt_u32 s4, 0x104
	s_cselect_b64 s[6:7], -1, 0
	s_and_b64 s[6:7], s[0:1], s[6:7]
	s_and_b64 vcc, exec, s[6:7]
	s_waitcnt lgkmcnt(6)
	v_mfma_f32_16x16x32_bf16 v[16:19], v[180:183], v[242:245], v[16:19]
	v_add_f32_e32 v220, v220, v75
	v_mfma_f32_16x16x32_bf16 v[20:23], v[180:183], v[204:207], v[20:23]
	v_add_f32_e32 v221, v221, v79
	ds_read_b128 v[176:179], v203 offset:12288
	s_waitcnt lgkmcnt(6)
	v_mfma_f32_16x16x32_bf16 v[84:87], v[230:233], v[124:127], v[84:87]
	v_cvt_pk_bf16_f32 v216, v64, v65
	v_mfma_f32_16x16x32_bf16 v[80:83], v[230:233], v[108:111], v[80:83]
	v_cvt_pk_bf16_f32 v217, v66, v67
	ds_read_b128 v[180:183], v210 offset:61440
	s_waitcnt lgkmcnt(6)
	v_mfma_f32_16x16x32_bf16 v[28:31], v[234:237], v[204:207], v[28:31]
	v_cvt_pk_bf16_f32 v238, v68, v69
	v_mfma_f32_16x16x32_bf16 v[24:27], v[234:237], v[242:245], v[24:27]
	v_cvt_pk_bf16_f32 v239, v70, v71
	ds_read_b128 v[230:233], v246 offset:12288
	s_waitcnt lgkmcnt(6)
	v_mfma_f32_16x16x32_bf16 v[88:91], v[160:163], v[96:99], 0
	v_exp_f32_e32 v80, v80
	v_exp_f32_e32 v84, v84
	v_mfma_f32_16x16x32_bf16 v[92:95], v[160:163], v[112:115], 0
	v_exp_f32_e32 v81, v81
	v_exp_f32_e32 v85, v85
	ds_read_b128 v[234:237], v210 offset:63488
	s_waitcnt lgkmcnt(6)
	v_mfma_f32_16x16x32_bf16 v[32:35], v[164:167], v[242:245], v[32:35]
	v_exp_f32_e32 v82, v82
	v_exp_f32_e32 v86, v86
	v_mfma_f32_16x16x32_bf16 v[36:39], v[164:167], v[204:207], v[36:39]
	v_exp_f32_e32 v83, v83
	v_exp_f32_e32 v87, v87
	s_waitcnt lgkmcnt(5)
	v_mfma_f32_16x16x32_bf16 v[92:95], v[168:171], v[116:119], v[92:95]
	v_add_f32_e32 v220, v220, v80
	v_mfma_f32_16x16x32_bf16 v[88:91], v[168:171], v[100:103], v[88:91]
	v_add_f32_e32 v221, v221, v84
	s_waitcnt lgkmcnt(4)
	v_mfma_f32_16x16x32_bf16 v[44:47], v[172:175], v[204:207], v[44:47]
	v_add_f32_e32 v220, v220, v81
	v_mfma_f32_16x16x32_bf16 v[40:43], v[172:175], v[242:245], v[40:43]
	v_add_f32_e32 v221, v221, v85
	s_waitcnt lgkmcnt(3)
	v_mfma_f32_16x16x32_bf16 v[88:91], v[176:179], v[104:107], v[88:91]
	v_add_f32_e32 v220, v220, v82
	v_mfma_f32_16x16x32_bf16 v[92:95], v[176:179], v[120:123], v[92:95]
	v_add_f32_e32 v221, v221, v86
	s_waitcnt lgkmcnt(2)
	v_mfma_f32_16x16x32_bf16 v[48:51], v[180:183], v[242:245], v[48:51]
	v_add_f32_e32 v220, v220, v83
	v_mfma_f32_16x16x32_bf16 v[52:55], v[180:183], v[204:207], v[52:55]
	v_add_f32_e32 v221, v221, v87
	s_waitcnt lgkmcnt(1)
	v_mfma_f32_16x16x32_bf16 v[92:95], v[230:233], v[124:127], v[92:95]
	v_cvt_pk_bf16_f32 v218, v72, v73
	v_mfma_f32_16x16x32_bf16 v[88:91], v[230:233], v[108:111], v[88:91]
	v_cvt_pk_bf16_f32 v219, v74, v75
	s_waitcnt lgkmcnt(0)
	v_mfma_f32_16x16x32_bf16 v[60:63], v[234:237], v[204:207], v[60:63]
	v_cvt_pk_bf16_f32 v240, v76, v77
	v_mfma_f32_16x16x32_bf16 v[56:59], v[234:237], v[242:245], v[56:59]
	v_cvt_pk_bf16_f32 v241, v78, v79
	s_cbranch_vccnz .LBB0_734
	s_waitcnt vmcnt(0)
	s_nop 7
	s_nop 7
	ds_swizzle_b32 v64, v194 offset:swizzle(SWAP,16)
	s_waitcnt lgkmcnt(0)
	v_add_f32_e32 v194, v194, v64
	v_mov_b32_e32 v65, v194
	s_nop 1
	v_permlane32_swap_b32_e32 v194, v65
	v_add_f32_e32 v194, v194, v65
	s_nop 0
	v_rcp_f32_e32 v66, v194
	ds_swizzle_b32 v64, v195 offset:swizzle(SWAP,16)
	s_waitcnt lgkmcnt(0)
	v_add_f32_e32 v195, v195, v64
	v_mov_b32_e32 v65, v195
	s_nop 1
	v_permlane32_swap_b32_e32 v195, v65
	v_add_f32_e32 v195, v195, v65
	s_nop 0
	v_rcp_f32_e32 v67, v195
	v_readlane_b32 s100, v250, 8
	v_mbcnt_lo_u32_b32 v68, -1, 0
	v_mbcnt_hi_u32_b32 v68, -1, v68
	v_and_b32_e32 v69, 15, v68
	v_lshrrev_b32_e32 v70, 4, v68
	s_lshr_b32 s101, s100, 1
	v_add_u32_e32 v69, s101, v69
	v_lshlrev_b32_e32 v69, 12, v69
	v_and_b32_e32 v71, 1, v70
	v_lshlrev_b32_e32 v71, 5, v71
	v_and_b32_e32 v70, 2, v70
	v_lshl_add_u32 v71, v70, 3, v71
	v_add_u32_e32 v70, v69, v71
	v_add_u32_e32 v71, 0x10000, v70
	v_mul_f32_e32 v0, v0, v66
	v_mul_f32_e32 v1, v1, v66
	v_mul_f32_e32 v2, v2, v66
	v_mul_f32_e32 v3, v3, v66
	v_mul_f32_e32 v8, v8, v66
	v_mul_f32_e32 v9, v9, v66
	v_mul_f32_e32 v10, v10, v66
	v_mul_f32_e32 v11, v11, v66
	v_cvt_pk_bf16_f32 v72, v0, v1
	v_cvt_pk_bf16_f32 v73, v2, v3
	v_cvt_pk_bf16_f32 v74, v8, v9
	v_cvt_pk_bf16_f32 v75, v10, v11
	s_nop 1
	v_permlane16_swap_b32_e32 v72, v74
	v_permlane16_swap_b32_e32 v73, v75
	s_nop 1
	global_store_dwordx4 v70, v[72:75], s[58:59] offset:0
	v_mul_f32_e32 v16, v16, v66
	v_mul_f32_e32 v17, v17, v66
	v_mul_f32_e32 v18, v18, v66
	v_mul_f32_e32 v19, v19, v66
	v_mul_f32_e32 v24, v24, v66
	v_mul_f32_e32 v25, v25, v66
	v_mul_f32_e32 v26, v26, v66
	v_mul_f32_e32 v27, v27, v66
	v_cvt_pk_bf16_f32 v76, v16, v17
	v_cvt_pk_bf16_f32 v77, v18, v19
	v_cvt_pk_bf16_f32 v78, v24, v25
	v_cvt_pk_bf16_f32 v79, v26, v27
	s_nop 1
	v_permlane16_swap_b32_e32 v76, v78
	v_permlane16_swap_b32_e32 v77, v79
	s_nop 1
	global_store_dwordx4 v70, v[76:79], s[58:59] offset:64
	v_mul_f32_e32 v32, v32, v66
	v_mul_f32_e32 v33, v33, v66
	v_mul_f32_e32 v34, v34, v66
	v_mul_f32_e32 v35, v35, v66
	v_mul_f32_e32 v40, v40, v66
	v_mul_f32_e32 v41, v41, v66
	v_mul_f32_e32 v42, v42, v66
	v_mul_f32_e32 v43, v43, v66
	v_cvt_pk_bf16_f32 v80, v32, v33
	v_cvt_pk_bf16_f32 v81, v34, v35
	v_cvt_pk_bf16_f32 v82, v40, v41
	v_cvt_pk_bf16_f32 v83, v42, v43
	s_nop 1
	v_permlane16_swap_b32_e32 v80, v82
	v_permlane16_swap_b32_e32 v81, v83
	s_nop 1
	global_store_dwordx4 v70, v[80:83], s[58:59] offset:128
	v_mul_f32_e32 v48, v48, v66
	v_mul_f32_e32 v49, v49, v66
	v_mul_f32_e32 v50, v50, v66
	v_mul_f32_e32 v51, v51, v66
	v_mul_f32_e32 v56, v56, v66
	v_mul_f32_e32 v57, v57, v66
	v_mul_f32_e32 v58, v58, v66
	v_mul_f32_e32 v59, v59, v66
	v_cvt_pk_bf16_f32 v84, v48, v49
	v_cvt_pk_bf16_f32 v85, v50, v51
	v_cvt_pk_bf16_f32 v86, v56, v57
	v_cvt_pk_bf16_f32 v87, v58, v59
	s_nop 1
	v_permlane16_swap_b32_e32 v84, v86
	v_permlane16_swap_b32_e32 v85, v87
	s_nop 1
	global_store_dwordx4 v70, v[84:87], s[58:59] offset:192
	v_mul_f32_e32 v4, v4, v67
	v_mul_f32_e32 v5, v5, v67
	v_mul_f32_e32 v6, v6, v67
	v_mul_f32_e32 v7, v7, v67
	v_mul_f32_e32 v12, v12, v67
	v_mul_f32_e32 v13, v13, v67
	v_mul_f32_e32 v14, v14, v67
	v_mul_f32_e32 v15, v15, v67
	v_cvt_pk_bf16_f32 v88, v4, v5
	v_cvt_pk_bf16_f32 v89, v6, v7
	v_cvt_pk_bf16_f32 v90, v12, v13
	v_cvt_pk_bf16_f32 v91, v14, v15
	s_nop 1
	v_permlane16_swap_b32_e32 v88, v90
	v_permlane16_swap_b32_e32 v89, v91
	s_nop 1
	global_store_dwordx4 v71, v[88:91], s[58:59] offset:0
	v_mul_f32_e32 v20, v20, v67
	v_mul_f32_e32 v21, v21, v67
	v_mul_f32_e32 v22, v22, v67
	v_mul_f32_e32 v23, v23, v67
	v_mul_f32_e32 v28, v28, v67
	v_mul_f32_e32 v29, v29, v67
	v_mul_f32_e32 v30, v30, v67
	v_mul_f32_e32 v31, v31, v67
	v_cvt_pk_bf16_f32 v92, v20, v21
	v_cvt_pk_bf16_f32 v93, v22, v23
	v_cvt_pk_bf16_f32 v94, v28, v29
	v_cvt_pk_bf16_f32 v95, v30, v31
	s_nop 1
	v_permlane16_swap_b32_e32 v92, v94
	v_permlane16_swap_b32_e32 v93, v95
	s_nop 1
	global_store_dwordx4 v71, v[92:95], s[58:59] offset:64
	v_mul_f32_e32 v36, v36, v67
	v_mul_f32_e32 v37, v37, v67
	v_mul_f32_e32 v38, v38, v67
	v_mul_f32_e32 v39, v39, v67
	v_mul_f32_e32 v44, v44, v67
	v_mul_f32_e32 v45, v45, v67
	v_mul_f32_e32 v46, v46, v67
	v_mul_f32_e32 v47, v47, v67
	v_cvt_pk_bf16_f32 v72, v36, v37
	v_cvt_pk_bf16_f32 v73, v38, v39
	v_cvt_pk_bf16_f32 v74, v44, v45
	v_cvt_pk_bf16_f32 v75, v46, v47
	s_nop 1
	v_permlane16_swap_b32_e32 v72, v74
	v_permlane16_swap_b32_e32 v73, v75
	s_nop 1
	global_store_dwordx4 v71, v[72:75], s[58:59] offset:128
	v_mul_f32_e32 v52, v52, v67
	v_mul_f32_e32 v53, v53, v67
	v_mul_f32_e32 v54, v54, v67
	v_mul_f32_e32 v55, v55, v67
	v_mul_f32_e32 v60, v60, v67
	v_mul_f32_e32 v61, v61, v67
	v_mul_f32_e32 v62, v62, v67
	v_mul_f32_e32 v63, v63, v67
	v_cvt_pk_bf16_f32 v76, v52, v53
	v_cvt_pk_bf16_f32 v77, v54, v55
	v_cvt_pk_bf16_f32 v78, v60, v61
	v_cvt_pk_bf16_f32 v79, v62, v63
	s_nop 1
	v_permlane16_swap_b32_e32 v76, v78
	v_permlane16_swap_b32_e32 v77, v79
	s_nop 1
	global_store_dwordx4 v71, v[76:79], s[58:59] offset:192
	s_barrier
